# v13 with both L2 warm-ups at 128B stride over two slices (redundant coverage)
# baseline (speedup 1.0000x reference)
_Z7k3_mainPKhPKfS2_S2_S2_PfS3_S3_:
	s_load_dwordx4 s[40:43], s[0:1], 0x0
	s_load_dwordx2 s[48:49], s[0:1], 0x10
	s_lshl_b32 s3, s2, 5
	s_and_b32 s3, s3, 0xe0
	s_lshr_b32 s2, s2, 3
	v_and_b32_e32 v128, 63, v0
	s_add_i32 s4, s3, s2
	s_waitcnt lgkmcnt(0)
	s_add_u32 s2, s40, 0x784000
	v_or_b32_e32 v134, 64, v128
	s_addc_u32 s3, s41, 0
	v_lshlrev_b32_e32 v98, 4, v128
	v_lshlrev_b32_e32 v1, 4, v134
	v_or_b32_e32 v133, 0x80, v128
	global_load_dwordx4 v[2:5], v98, s[2:3]
	global_load_dwordx4 v[6:9], v1, s[2:3]
	v_lshlrev_b32_e32 v1, 4, v133
	global_load_dwordx4 v[10:13], v1, s[2:3]
	v_or_b32_e32 v1, 0xc00, v98
	global_load_dwordx4 v[42:45], v1, s[2:3]
	s_load_dwordx2 s[2:3], s[0:1], 0x20
	v_lshrrev_b32_e32 v150, 6, v0
	s_lshl_b32 s33, s4, 4
	v_or_b32_e32 v66, s33, v150
	v_ashrrev_i32_e32 v67, 31, v66
	v_lshlrev_b64 v[14:15], 12, v[66:67]
	v_mov_b32_e32 v99, 0
	s_waitcnt lgkmcnt(0)
	v_lshl_add_u64 v[14:15], s[2:3], 0, v[14:15]
	v_lshl_add_u64 v[14:15], v[14:15], 0, v[98:99]
	global_load_dwordx4 v[54:57], v[14:15], off
	global_load_dwordx4 v[58:61], v[14:15], off offset:1024
	global_load_dwordx4 v[62:65], v[14:15], off offset:2048
	s_lshr_b32 s59, s33, 4
	s_and_b32 s59, s59, 31
	s_lshl_b32 s59, s59, 15
	s_add_u32 s59, s59, 0x787000
	s_add_u32 s68, s40, s59
	s_addc_u32 s69, s41, 0
	v_lshlrev_b32_e32 v207, 7, v0
	global_load_dword v207, v207, s[68:69]
	s_movk_i32 s4, 0xc00
	v_mov_b64_e32 v[16:17], s[42:43]
	v_mad_i64_i32 v[18:19], s[6:7], v66, s4, v[16:17]
	v_lshl_add_u64 v[18:19], v[18:19], 0, v[98:99]
	global_load_dwordx4 v[38:41], v[18:19], off
	global_load_dwordx4 v[34:37], v[18:19], off offset:1024
	global_load_dwordx4 v[30:33], v[18:19], off offset:2048
	global_load_dwordx4 v[68:71], v[14:15], off offset:3072
	v_mov_b32_e32 v50, v99
	v_mov_b32_e32 v51, v99
	v_mov_b32_e32 v52, v99
	v_mbcnt_lo_u32_b32 v1, -1, 0
	v_mov_b32_e32 v53, v99
	v_mbcnt_hi_u32_b32 v129, -1, v1
	v_and_b32_e32 v132, 64, v129
	v_xor_b32_e32 v1, 16, v129
	v_add_u32_e32 v130, 64, v132
	s_mov_b32 s5, 0xff61b1e6
	v_cmp_lt_i32_e32 vcc, v1, v130
	v_lshlrev_b32_e32 v135, 2, v128
	v_or_b32_e32 v146, 1, v135
	v_cndmask_b32_e32 v1, v129, v1, vcc
	v_or_b32_e32 v148, 2, v135
	v_or_b32_e32 v149, 3, v135
	v_or_b32_e32 v147, 0x100, v135
	v_or_b32_e32 v152, 0x101, v135
	v_or_b32_e32 v153, 0x102, v135
	v_or_b32_e32 v137, 0x103, v135
	v_or_b32_e32 v136, 0x200, v135
	v_or_b32_e32 v138, 0x201, v135
	v_or_b32_e32 v140, 0x202, v135
	v_or_b32_e32 v141, 0x203, v135
	v_or_b32_e32 v139, 0x300, v135
	v_or_b32_e32 v143, 0x301, v135
	v_or_b32_e32 v144, 0x302, v135
	s_add_u32 s50, s40, 0x780000
	s_addc_u32 s51, s41, 0
	v_or_b32_e32 v145, 0x303, v135
	v_lshl_add_u64 v[22:23], v[66:67], 2, s[50:51]
	global_load_dword v67, v[22:23], off
	v_lshlrev_b32_e32 v1, 2, v1
	v_or_b32_e32 v20, 8, v66
	v_ashrrev_i32_e32 v21, 31, v20
	v_mad_i64_i32 v[16:17], s[6:7], v20, s4, v[16:17]
	v_lshlrev_b64 v[18:19], 12, v[20:21]
	v_lshl_add_u64 v[46:47], v[16:17], 0, v[98:99]
	v_lshl_add_u64 v[16:17], s[2:3], 0, v[18:19]
	v_lshl_add_u64 v[48:49], v[16:17], 0, v[98:99]
	global_load_dwordx4 v[26:29], v[48:49], off
	global_load_dwordx4 v[22:25], v[48:49], off offset:1024
	global_load_dwordx4 v[18:21], v[48:49], off offset:2048
	global_load_dwordx4 v[14:17], v[48:49], off offset:3072
	s_waitcnt vmcnt(15)
	v_max_f32_e32 v5, v5, v5
	v_max_f32_e32 v4, v4, v4
	s_waitcnt vmcnt(14)
	v_max_f32_e32 v9, v9, v9
	v_max_f32_e32 v8, v8, v8
	s_waitcnt vmcnt(13)
	v_max_f32_e32 v13, v13, v13
	v_max_f32_e32 v12, v12, v12
	s_waitcnt vmcnt(12)
	v_max_f32_e32 v45, v45, v45
	v_max_f32_e32 v44, v44, v44
	v_max_f32_e32 v4, v4, v5
	v_max_f32_e32 v5, v8, v9
	v_max_f32_e32 v8, v12, v13
	v_max_f32_e32 v9, v44, v45
	v_max3_f32 v2, v2, v3, v4
	v_max3_f32 v3, v6, v7, v5
	v_max3_f32 v4, v10, v11, v8
	v_max3_f32 v5, v42, v43, v9
	v_max3_f32 v2, v2, 0, v3
	v_max3_f32 v2, v2, v4, v5
	s_waitcnt vmcnt(11)
	v_cmp_lt_f32_e32 vcc, s5, v54
	v_mov_b32_dpp v50, v2 row_ror:1 row_mask:0xf bank_mask:0xf
	v_max_f32_e32 v4, v50, v50
	v_max_f32_e32 v2, v2, v4
	v_cndmask_b32_e32 v3, 0, v135, vcc
	s_nop 0
	v_mov_b32_dpp v51, v2 row_ror:2 row_mask:0xf bank_mask:0xf
	v_max_f32_e32 v4, v51, v51
	v_max_f32_e32 v2, v2, v4
	s_nop 1
	v_mov_b32_dpp v52, v2 row_ror:4 row_mask:0xf bank_mask:0xf
	v_max_f32_e32 v4, v52, v52
	v_max_f32_e32 v2, v2, v4
	s_nop 1
	v_mov_b32_dpp v53, v2 row_ror:8 row_mask:0xf bank_mask:0xf
	v_max_f32_e32 v4, v53, v53
	v_max_f32_e32 v42, v2, v4
	v_max_f32_e32 v2, v54, v54
	v_max_f32_e32 v2, 0xff61b1e6, v2
	v_cmp_gt_f32_e32 vcc, v55, v2
	v_xor_b32_e32 v4, 32, v129
	ds_bpermute_b32 v43, v1, v42
	v_cndmask_b32_e32 v2, v2, v55, vcc
	v_cndmask_b32_e32 v3, v3, v146, vcc
	v_cmp_gt_f32_e32 vcc, v56, v2
	s_waitcnt lgkmcnt(0)
	v_max_f32_e32 v43, v43, v43
	v_cndmask_b32_e32 v2, v2, v56, vcc
	v_cndmask_b32_e32 v3, v3, v148, vcc
	v_cmp_gt_f32_e32 vcc, v57, v2
	v_max_f32_e32 v75, v42, v43
	v_mov_b64_e32 v[42:43], s[48:49]
	v_cndmask_b32_e32 v2, v2, v57, vcc
	v_cndmask_b32_e32 v3, v3, v149, vcc
	s_waitcnt vmcnt(10)
	v_cmp_gt_f32_e32 vcc, v58, v2
	s_nop 1
	v_cndmask_b32_e32 v2, v2, v58, vcc
	v_cndmask_b32_e32 v3, v3, v147, vcc
	v_cmp_gt_f32_e32 vcc, v59, v2
	s_nop 1
	v_cndmask_b32_e32 v2, v2, v59, vcc
	v_cndmask_b32_e32 v3, v3, v152, vcc
	v_cmp_gt_f32_e32 vcc, v60, v2
	s_nop 1
	v_cndmask_b32_e32 v2, v2, v60, vcc
	v_cndmask_b32_e32 v3, v3, v153, vcc
	v_cmp_gt_f32_e32 vcc, v61, v2
	s_nop 1
	v_cndmask_b32_e32 v2, v2, v61, vcc
	v_cndmask_b32_e32 v3, v3, v137, vcc
	s_waitcnt vmcnt(9)
	v_cmp_gt_f32_e32 vcc, v62, v2
	s_nop 1
	v_cndmask_b32_e32 v2, v2, v62, vcc
	v_cndmask_b32_e32 v3, v3, v136, vcc
	v_cmp_gt_f32_e32 vcc, v63, v2
	s_nop 1
	v_cndmask_b32_e32 v2, v2, v63, vcc
	v_cndmask_b32_e32 v3, v3, v138, vcc
	v_cmp_gt_f32_e32 vcc, v64, v2
	s_nop 1
	v_cndmask_b32_e32 v2, v2, v64, vcc
	v_cndmask_b32_e32 v3, v3, v140, vcc
	v_cmp_gt_f32_e32 vcc, v65, v2
	s_nop 1
	v_cndmask_b32_e32 v2, v2, v65, vcc
	v_cndmask_b32_e32 v3, v3, v141, vcc
	s_waitcnt vmcnt(5)
	v_cmp_gt_f32_e32 vcc, v68, v2
	s_nop 1
	v_cndmask_b32_e32 v2, v2, v68, vcc
	v_cndmask_b32_e32 v3, v3, v139, vcc
	v_cmp_gt_f32_e32 vcc, v69, v2
	s_nop 1
	v_cndmask_b32_e32 v2, v2, v69, vcc
	v_cndmask_b32_e32 v3, v3, v143, vcc
	v_cmp_gt_f32_e32 vcc, v70, v2
	s_nop 1
	v_cndmask_b32_e32 v2, v2, v70, vcc
	v_cndmask_b32_e32 v3, v3, v144, vcc
	v_cmp_gt_f32_e32 vcc, v71, v2
	s_nop 1
	v_cndmask_b32_e32 v45, v2, v71, vcc
	v_mov_b32_e32 v2, v99
	v_cndmask_b32_e32 v44, v3, v145, vcc
	v_max_f32_e32 v3, v45, v45
	v_mov_b32_dpp v2, v45 row_ror:1 row_mask:0xf bank_mask:0xf
	v_max_f32_e32 v2, v2, v2
	v_max_f32_e32 v2, v3, v2
	v_mov_b32_e32 v3, v99
	v_cmp_lt_i32_e32 vcc, v4, v130
	s_nop 0
	v_mov_b32_dpp v3, v2 row_ror:2 row_mask:0xf bank_mask:0xf
	v_max_f32_e32 v3, v3, v3
	v_max_f32_e32 v2, v2, v3
	v_mov_b32_e32 v3, v99
	v_cndmask_b32_e32 v4, v129, v4, vcc
	v_lshlrev_b32_e32 v151, 2, v4
	v_mov_b32_dpp v3, v2 row_ror:4 row_mask:0xf bank_mask:0xf
	v_max_f32_e32 v3, v3, v3
	v_max_f32_e32 v2, v2, v3
	v_mov_b32_e32 v3, v99
	ds_bpermute_b32 v76, v151, v75
	s_nop 0
	v_mov_b32_dpp v3, v2 row_ror:8 row_mask:0xf bank_mask:0xf
	v_max_f32_e32 v3, v3, v3
	v_max_f32_e32 v2, v2, v3
	ds_bpermute_b32 v3, v1, v2
	s_waitcnt lgkmcnt(0)
	v_max_f32_e32 v3, v3, v3
	v_max_f32_e32 v48, v2, v3
	ds_bpermute_b32 v49, v151, v48
	global_load_dwordx4 v[10:13], v[46:47], off
	global_load_dwordx4 v[6:9], v[46:47], off offset:1024
	global_load_dwordx4 v[2:5], v[46:47], off offset:2048
	s_waitcnt lgkmcnt(0)
	v_max_f32_e32 v46, v49, v49
	v_max_f32_e32 v74, v48, v46
	v_cmp_eq_f32_e32 vcc, v45, v74
	s_ff1_i32_b64 s2, vcc
	s_cmp_lg_u64 vcc, 0
	s_cselect_b32 s2, s2, 63
	v_or_b32_e32 v45, s2, v132
	v_lshlrev_b32_e32 v45, 2, v45
	ds_bpermute_b32 v44, v45, v44
	s_waitcnt lgkmcnt(0)
	v_mad_i64_i32 v[42:43], s[2:3], v44, s4, v[42:43]
	v_lshl_add_u64 v[72:73], v[42:43], 0, v[98:99]
	global_load_dwordx4 v[42:45], v[72:73], off
	global_load_dwordx4 v[46:49], v[72:73], off offset:1024
	global_load_dwordx4 v[50:53], v[72:73], off offset:2048
	v_max_f32_e32 v72, v76, v76
	v_max_f32_e32 v142, v75, v72
	s_waitcnt vmcnt(10)
	v_mul_f32_e32 v67, v142, v67
	s_mov_b32 s2, 0xf800000
	v_mul_f32_e32 v72, 0x4f800000, v67
	v_cmp_gt_f32_e32 vcc, s2, v67
	v_mad_i64_i32 v[90:91], s[2:3], v66, s4, 0
	s_nop 0
	v_cndmask_b32_e32 v67, v67, v72, vcc
	v_sqrt_f32_e32 v72, v67
	v_mov_b32_e32 v66, 0x1c000
	v_cmp_eq_u32_e64 s[2:3], 0, v128
	v_lshl_or_b32 v131, v150, 8, v66
	v_add_u32_e32 v73, -1, v72
	v_fma_f32 v75, -v73, v72, v67
	v_cmp_ge_f32_e64 s[4:5], 0, v75
	v_add_u32_e32 v75, 1, v72
	s_nop 0
	v_cndmask_b32_e64 v73, v72, v73, s[4:5]
	v_fma_f32 v72, -v75, v72, v67
	v_cmp_lt_f32_e64 s[4:5], 0, v72
	s_nop 1
	v_cndmask_b32_e64 v72, v73, v75, s[4:5]
	v_mul_f32_e32 v73, 0x37800000, v72
	v_cndmask_b32_e32 v72, v72, v73, vcc
	v_mov_b32_e32 v73, 0x260
	v_cmp_class_f32_e32 vcc, v67, v73
	s_nop 1
	v_cndmask_b32_e32 v67, v72, v67, vcc
	v_fmamk_f32 v67, v67, 0xbbb8cfc0, v74
	v_cmp_ge_f32_e64 s[36:37], v54, v67
	v_cmp_ge_f32_e64 s[34:35], v55, v67
	s_bcnt1_i32_b64 s4, s[36:37]
	s_bcnt1_i32_b64 s5, s[34:35]
	v_cmp_ge_f32_e64 s[30:31], v56, v67
	s_add_i32 s4, s4, s5
	s_bcnt1_i32_b64 s5, s[30:31]
	v_cmp_ge_f32_e64 s[28:29], v57, v67
	s_add_i32 s4, s4, s5
	s_bcnt1_i32_b64 s5, s[28:29]
	v_cmp_ge_f32_e64 s[26:27], v58, v67
	s_add_i32 s4, s4, s5
	s_bcnt1_i32_b64 s5, s[26:27]
	v_cmp_ge_f32_e64 s[24:25], v59, v67
	s_add_i32 s4, s4, s5
	s_bcnt1_i32_b64 s5, s[24:25]
	v_cmp_ge_f32_e64 s[22:23], v60, v67
	s_add_i32 s4, s4, s5
	s_bcnt1_i32_b64 s5, s[22:23]
	v_cmp_ge_f32_e64 s[20:21], v61, v67
	s_add_i32 s4, s4, s5
	s_bcnt1_i32_b64 s5, s[20:21]
	v_cmp_ge_f32_e64 s[18:19], v62, v67
	s_add_i32 s4, s4, s5
	s_bcnt1_i32_b64 s5, s[18:19]
	v_cmp_ge_f32_e64 s[16:17], v63, v67
	s_add_i32 s4, s4, s5
	s_bcnt1_i32_b64 s5, s[16:17]
	v_cmp_ge_f32_e64 s[14:15], v64, v67
	s_add_i32 s4, s4, s5
	s_bcnt1_i32_b64 s5, s[14:15]
	v_cmp_ge_f32_e64 s[12:13], v65, v67
	s_add_i32 s4, s4, s5
	s_bcnt1_i32_b64 s5, s[12:13]
	v_cmp_ge_f32_e64 s[10:11], v68, v67
	s_add_i32 s4, s4, s5
	s_bcnt1_i32_b64 s5, s[10:11]
	v_cmp_ge_f32_e64 s[8:9], v69, v67
	s_add_i32 s4, s4, s5
	s_bcnt1_i32_b64 s5, s[8:9]
	v_cmp_ge_f32_e64 s[6:7], v70, v67
	s_add_i32 s4, s4, s5
	s_bcnt1_i32_b64 s5, s[6:7]
	s_add_i32 s38, s4, s5
	v_cmp_ge_f32_e64 s[4:5], v71, v67
	s_bcnt1_i32_b64 s39, s[4:5]
	s_add_i32 s38, s38, s39
	s_cmpk_lt_u32 s38, 0x41
	s_cbranch_scc0 .LBB2_7
	s_cmp_gt_u32 s38, 1
	s_waitcnt vmcnt(0)
	v_mov_b64_e32 v[56:57], v[52:53]
	v_mov_b64_e32 v[54:55], v[50:51]
	v_mov_b64_e32 v[60:61], v[48:49]
	v_mov_b64_e32 v[58:59], v[46:47]
	v_mov_b64_e32 v[64:65], v[44:45]
	v_mov_b64_e32 v[62:63], v[42:43]
	s_cbranch_scc0 .LBB2_94
	v_cndmask_b32_e64 v54, 0, 1, s[36:37]
	s_mov_b32 s42, 0
	v_cmp_ne_u32_e32 vcc, 0, v54
	s_cbranch_vccz .LBB2_8
	v_mov_b32_e32 v54, 0x1c000
	v_lshl_or_b32 v54, v150, 8, v54
	s_branch .LBB2_5
